# v33 + route phase: table-fragment LDS reads pipelined six deep (six quads, counted lgkmcnt) instead of one read-wait-MFMA at a time
# baseline (speedup 1.0000x reference)
; #define LAS __attribute__((address_space(3)))
; __device__ __forceinline__ void phase_route(Frame& F, int l, bool dummy = false) {
;     ...
;         for (int pass = 0; pass < 2; ++pass) {
;             asm volatile("s_waitcnt vmcnt(0)" ::: "memory"); __syncthreads();
;             const LAS unsigned char* tb = F.lds + (size_t)ri * (RT_PITCH * 2) + kq * 16;
; #pragma unroll
;             for (int sI = 0; sI < 32; ++sI) {
; #pragma unroll
;                 for (int blk = 0; blk < 3; ++blk) { const int cb = blk < 2 ? blk * 16 : 20;
;                     const bf16x8 bfr = *(const LAS bf16x8*)(tb + (size_t)cb * (RT_PITCH * 2) + sI * 64);
;                     acc[blk] = __builtin_amdgcn_mfma_f32_16x16x32_bf16(af[sI], bfr, acc[blk], 0, 0, 0); }
;             }
.LBB0_1033:
	s_waitcnt vmcnt(0)
	s_barrier
	ds_read_b128 v[176:179], v159
	ds_read_b128 v[180:183], v159 offset:33024
	ds_read_b128 v[184:187], v159 offset:41280
	ds_read_b128 v[190:193], v159 offset:64
	ds_read_b128 v[194:197], v159 offset:33088
	ds_read_b128 v[198:201], v159 offset:41344
	s_xor_b64 s[20:21], s[22:23], -1
	s_and_b64 vcc, exec, s[20:21]
	s_mov_b64 s[22:23], -1
	s_waitcnt lgkmcnt(5)
	v_mfma_f32_16x16x32_bf16 v[130:133], v[2:5], v[176:179], v[130:133]
	ds_read_b128 v[176:179], v159 offset:128
	s_waitcnt lgkmcnt(5)
	v_mfma_f32_16x16x32_bf16 v[134:137], v[2:5], v[180:183], v[134:137]
	ds_read_b128 v[180:183], v159 offset:33152
	s_waitcnt lgkmcnt(5)
	v_mfma_f32_16x16x32_bf16 v[138:141], v[2:5], v[184:187], v[138:141]
	ds_read_b128 v[184:187], v159 offset:41408
	s_waitcnt lgkmcnt(5)
	v_mfma_f32_16x16x32_bf16 v[130:133], v[6:9], v[190:193], v[130:133]
	ds_read_b128 v[190:193], v159 offset:192
	s_waitcnt lgkmcnt(5)
	v_mfma_f32_16x16x32_bf16 v[134:137], v[6:9], v[194:197], v[134:137]
	ds_read_b128 v[194:197], v159 offset:33216
	s_waitcnt lgkmcnt(5)
	v_mfma_f32_16x16x32_bf16 v[138:141], v[6:9], v[198:201], v[138:141]
	ds_read_b128 v[198:201], v159 offset:41472
	s_waitcnt lgkmcnt(5)
	v_mfma_f32_16x16x32_bf16 v[130:133], v[10:13], v[176:179], v[130:133]
	ds_read_b128 v[176:179], v159 offset:256
	s_waitcnt lgkmcnt(5)
	v_mfma_f32_16x16x32_bf16 v[134:137], v[10:13], v[180:183], v[134:137]
	ds_read_b128 v[180:183], v159 offset:33280
	s_waitcnt lgkmcnt(5)
	v_mfma_f32_16x16x32_bf16 v[138:141], v[10:13], v[184:187], v[138:141]
	ds_read_b128 v[184:187], v159 offset:41536
	s_waitcnt lgkmcnt(5)
	v_mfma_f32_16x16x32_bf16 v[130:133], v[14:17], v[190:193], v[130:133]
	ds_read_b128 v[190:193], v159 offset:320
	s_waitcnt lgkmcnt(5)
	v_mfma_f32_16x16x32_bf16 v[134:137], v[14:17], v[194:197], v[134:137]
	ds_read_b128 v[194:197], v159 offset:33344
	s_waitcnt lgkmcnt(5)
	v_mfma_f32_16x16x32_bf16 v[138:141], v[14:17], v[198:201], v[138:141]
	ds_read_b128 v[198:201], v159 offset:41600
	s_waitcnt lgkmcnt(5)
	v_mfma_f32_16x16x32_bf16 v[130:133], v[18:21], v[176:179], v[130:133]
	ds_read_b128 v[176:179], v159 offset:384
	s_waitcnt lgkmcnt(5)
	v_mfma_f32_16x16x32_bf16 v[134:137], v[18:21], v[180:183], v[134:137]
	ds_read_b128 v[180:183], v159 offset:33408
	s_waitcnt lgkmcnt(5)
	v_mfma_f32_16x16x32_bf16 v[138:141], v[18:21], v[184:187], v[138:141]
	ds_read_b128 v[184:187], v159 offset:41664
	s_waitcnt lgkmcnt(5)
	v_mfma_f32_16x16x32_bf16 v[130:133], v[22:25], v[190:193], v[130:133]
	ds_read_b128 v[190:193], v159 offset:448
	s_waitcnt lgkmcnt(5)
	v_mfma_f32_16x16x32_bf16 v[134:137], v[22:25], v[194:197], v[134:137]
	ds_read_b128 v[194:197], v159 offset:33472
	s_waitcnt lgkmcnt(5)
	v_mfma_f32_16x16x32_bf16 v[138:141], v[22:25], v[198:201], v[138:141]
	ds_read_b128 v[198:201], v159 offset:41728
	s_waitcnt lgkmcnt(5)
	v_mfma_f32_16x16x32_bf16 v[130:133], v[26:29], v[176:179], v[130:133]
	ds_read_b128 v[176:179], v159 offset:512
	s_waitcnt lgkmcnt(5)
	v_mfma_f32_16x16x32_bf16 v[134:137], v[26:29], v[180:183], v[134:137]
	ds_read_b128 v[180:183], v159 offset:33536
	s_waitcnt lgkmcnt(5)
	v_mfma_f32_16x16x32_bf16 v[138:141], v[26:29], v[184:187], v[138:141]
	ds_read_b128 v[184:187], v159 offset:41792
	s_waitcnt lgkmcnt(5)
	v_mfma_f32_16x16x32_bf16 v[130:133], v[30:33], v[190:193], v[130:133]
	ds_read_b128 v[190:193], v159 offset:576
	s_waitcnt lgkmcnt(5)
	v_mfma_f32_16x16x32_bf16 v[134:137], v[30:33], v[194:197], v[134:137]
	ds_read_b128 v[194:197], v159 offset:33600
	s_waitcnt lgkmcnt(5)
	v_mfma_f32_16x16x32_bf16 v[138:141], v[30:33], v[198:201], v[138:141]
	ds_read_b128 v[198:201], v159 offset:41856
	s_waitcnt lgkmcnt(5)
	v_mfma_f32_16x16x32_bf16 v[130:133], v[34:37], v[176:179], v[130:133]
	ds_read_b128 v[176:179], v159 offset:640
	s_waitcnt lgkmcnt(5)
	v_mfma_f32_16x16x32_bf16 v[134:137], v[34:37], v[180:183], v[134:137]
	ds_read_b128 v[180:183], v159 offset:33664
	s_waitcnt lgkmcnt(5)
	v_mfma_f32_16x16x32_bf16 v[138:141], v[34:37], v[184:187], v[138:141]
	ds_read_b128 v[184:187], v159 offset:41920
	s_waitcnt lgkmcnt(5)
	v_mfma_f32_16x16x32_bf16 v[130:133], v[38:41], v[190:193], v[130:133]
	ds_read_b128 v[190:193], v159 offset:704
	s_waitcnt lgkmcnt(5)
	v_mfma_f32_16x16x32_bf16 v[134:137], v[38:41], v[194:197], v[134:137]
	ds_read_b128 v[194:197], v159 offset:33728
	s_waitcnt lgkmcnt(5)
	v_mfma_f32_16x16x32_bf16 v[138:141], v[38:41], v[198:201], v[138:141]
	ds_read_b128 v[198:201], v159 offset:41984
	s_waitcnt lgkmcnt(5)
	v_mfma_f32_16x16x32_bf16 v[130:133], v[42:45], v[176:179], v[130:133]
	ds_read_b128 v[176:179], v159 offset:768
	s_waitcnt lgkmcnt(5)
	v_mfma_f32_16x16x32_bf16 v[134:137], v[42:45], v[180:183], v[134:137]
	ds_read_b128 v[180:183], v159 offset:33792
	s_waitcnt lgkmcnt(5)
	v_mfma_f32_16x16x32_bf16 v[138:141], v[42:45], v[184:187], v[138:141]
	ds_read_b128 v[184:187], v159 offset:42048
	s_waitcnt lgkmcnt(5)
	v_mfma_f32_16x16x32_bf16 v[130:133], v[46:49], v[190:193], v[130:133]
	ds_read_b128 v[190:193], v159 offset:832
	s_waitcnt lgkmcnt(5)
	v_mfma_f32_16x16x32_bf16 v[134:137], v[46:49], v[194:197], v[134:137]
	ds_read_b128 v[194:197], v159 offset:33856
	s_waitcnt lgkmcnt(5)
	v_mfma_f32_16x16x32_bf16 v[138:141], v[46:49], v[198:201], v[138:141]
	ds_read_b128 v[198:201], v159 offset:42112
	s_waitcnt lgkmcnt(5)
	v_mfma_f32_16x16x32_bf16 v[130:133], v[50:53], v[176:179], v[130:133]
	ds_read_b128 v[176:179], v159 offset:896
	s_waitcnt lgkmcnt(5)
	v_mfma_f32_16x16x32_bf16 v[134:137], v[50:53], v[180:183], v[134:137]
	ds_read_b128 v[180:183], v159 offset:33920
	s_waitcnt lgkmcnt(5)
	v_mfma_f32_16x16x32_bf16 v[138:141], v[50:53], v[184:187], v[138:141]
	ds_read_b128 v[184:187], v159 offset:42176
	s_waitcnt lgkmcnt(5)
; #define LAS __attribute__((address_space(3)))
; __device__ __forceinline__ void phase_route(Frame& F, int l, bool dummy = false) {
;     ...
;         for (int pass = 0; pass < 2; ++pass) {
;             asm volatile("s_waitcnt vmcnt(0)" ::: "memory"); __syncthreads();
;             const LAS unsigned char* tb = F.lds + (size_t)ri * (RT_PITCH * 2) + kq * 16;
; #pragma unroll
;             for (int sI = 0; sI < 32; ++sI) {
; #pragma unroll
;                 for (int blk = 0; blk < 3; ++blk) { const int cb = blk < 2 ? blk * 16 : 20;
;                     const bf16x8 bfr = *(const LAS bf16x8*)(tb + (size_t)cb * (RT_PITCH * 2) + sI * 64);
;                     acc[blk] = __builtin_amdgcn_mfma_f32_16x16x32_bf16(af[sI], bfr, acc[blk], 0, 0, 0); }
;             }
	v_mfma_f32_16x16x32_bf16 v[130:133], v[54:57], v[190:193], v[130:133]
	ds_read_b128 v[190:193], v159 offset:960
	s_waitcnt lgkmcnt(5)
	v_mfma_f32_16x16x32_bf16 v[134:137], v[54:57], v[194:197], v[134:137]
	ds_read_b128 v[194:197], v159 offset:33984
	s_waitcnt lgkmcnt(5)
	v_mfma_f32_16x16x32_bf16 v[138:141], v[54:57], v[198:201], v[138:141]
	ds_read_b128 v[198:201], v159 offset:42240
	s_waitcnt lgkmcnt(5)
	v_mfma_f32_16x16x32_bf16 v[130:133], v[58:61], v[176:179], v[130:133]
	ds_read_b128 v[176:179], v159 offset:1024
	s_waitcnt lgkmcnt(5)
	v_mfma_f32_16x16x32_bf16 v[134:137], v[58:61], v[180:183], v[134:137]
	ds_read_b128 v[180:183], v159 offset:34048
	s_waitcnt lgkmcnt(5)
	v_mfma_f32_16x16x32_bf16 v[138:141], v[58:61], v[184:187], v[138:141]
	ds_read_b128 v[184:187], v159 offset:42304
	s_waitcnt lgkmcnt(5)
	v_mfma_f32_16x16x32_bf16 v[130:133], v[62:65], v[190:193], v[130:133]
	ds_read_b128 v[190:193], v159 offset:1088
	s_waitcnt lgkmcnt(5)
	v_mfma_f32_16x16x32_bf16 v[134:137], v[62:65], v[194:197], v[134:137]
	ds_read_b128 v[194:197], v159 offset:34112
	s_waitcnt lgkmcnt(5)
	v_mfma_f32_16x16x32_bf16 v[138:141], v[62:65], v[198:201], v[138:141]
	ds_read_b128 v[198:201], v159 offset:42368
	s_waitcnt lgkmcnt(5)
	v_mfma_f32_16x16x32_bf16 v[130:133], v[66:69], v[176:179], v[130:133]
	ds_read_b128 v[176:179], v159 offset:1152
	s_waitcnt lgkmcnt(5)
	v_mfma_f32_16x16x32_bf16 v[134:137], v[66:69], v[180:183], v[134:137]
	ds_read_b128 v[180:183], v159 offset:34176
	s_waitcnt lgkmcnt(5)
	v_mfma_f32_16x16x32_bf16 v[138:141], v[66:69], v[184:187], v[138:141]
	ds_read_b128 v[184:187], v159 offset:42432
	s_waitcnt lgkmcnt(5)
	v_mfma_f32_16x16x32_bf16 v[130:133], v[70:73], v[190:193], v[130:133]
	ds_read_b128 v[190:193], v159 offset:1216
	s_waitcnt lgkmcnt(5)
	v_mfma_f32_16x16x32_bf16 v[134:137], v[70:73], v[194:197], v[134:137]
	ds_read_b128 v[194:197], v159 offset:34240
	s_waitcnt lgkmcnt(5)
	v_mfma_f32_16x16x32_bf16 v[138:141], v[70:73], v[198:201], v[138:141]
	ds_read_b128 v[198:201], v159 offset:42496
	s_waitcnt lgkmcnt(5)
	v_mfma_f32_16x16x32_bf16 v[130:133], v[74:77], v[176:179], v[130:133]
	ds_read_b128 v[176:179], v159 offset:1280
	s_waitcnt lgkmcnt(5)
	v_mfma_f32_16x16x32_bf16 v[134:137], v[74:77], v[180:183], v[134:137]
	ds_read_b128 v[180:183], v159 offset:34304
	s_waitcnt lgkmcnt(5)
	v_mfma_f32_16x16x32_bf16 v[138:141], v[74:77], v[184:187], v[138:141]
	ds_read_b128 v[184:187], v159 offset:42560
	s_waitcnt lgkmcnt(5)
	v_mfma_f32_16x16x32_bf16 v[130:133], v[78:81], v[190:193], v[130:133]
	ds_read_b128 v[190:193], v159 offset:1344
	s_waitcnt lgkmcnt(5)
	v_mfma_f32_16x16x32_bf16 v[134:137], v[78:81], v[194:197], v[134:137]
	ds_read_b128 v[194:197], v159 offset:34368
	s_waitcnt lgkmcnt(5)
	v_mfma_f32_16x16x32_bf16 v[138:141], v[78:81], v[198:201], v[138:141]
	ds_read_b128 v[198:201], v159 offset:42624
	s_waitcnt lgkmcnt(5)
	v_mfma_f32_16x16x32_bf16 v[130:133], v[82:85], v[176:179], v[130:133]
	ds_read_b128 v[176:179], v159 offset:1408
	s_waitcnt lgkmcnt(5)
	v_mfma_f32_16x16x32_bf16 v[134:137], v[82:85], v[180:183], v[134:137]
	ds_read_b128 v[180:183], v159 offset:34432
	s_waitcnt lgkmcnt(5)
	v_mfma_f32_16x16x32_bf16 v[138:141], v[82:85], v[184:187], v[138:141]
	ds_read_b128 v[184:187], v159 offset:42688
	s_waitcnt lgkmcnt(5)
	v_mfma_f32_16x16x32_bf16 v[130:133], v[86:89], v[190:193], v[130:133]
	ds_read_b128 v[190:193], v159 offset:1472
	s_waitcnt lgkmcnt(5)
	v_mfma_f32_16x16x32_bf16 v[134:137], v[86:89], v[194:197], v[134:137]
	ds_read_b128 v[194:197], v159 offset:34496
	s_waitcnt lgkmcnt(5)
	v_mfma_f32_16x16x32_bf16 v[138:141], v[86:89], v[198:201], v[138:141]
	ds_read_b128 v[198:201], v159 offset:42752
	s_waitcnt lgkmcnt(5)
	v_mfma_f32_16x16x32_bf16 v[130:133], v[90:93], v[176:179], v[130:133]
	ds_read_b128 v[176:179], v159 offset:1536
	s_waitcnt lgkmcnt(5)
; #define LAS __attribute__((address_space(3)))
; __device__ __forceinline__ void phase_route(Frame& F, int l, bool dummy = false) {
;     ...
;             const LAS unsigned char* tb = F.lds + (size_t)ri * (RT_PITCH * 2) + kq * 16;
; #pragma unroll
;             for (int sI = 0; sI < 32; ++sI) {
; #pragma unroll
;                 for (int blk = 0; blk < 3; ++blk) { const int cb = blk < 2 ? blk * 16 : 20;
;                     const bf16x8 bfr = *(const LAS bf16x8*)(tb + (size_t)cb * (RT_PITCH * 2) + sI * 64);
;                     acc[blk] = __builtin_amdgcn_mfma_f32_16x16x32_bf16(af[sI], bfr, acc[blk], 0, 0, 0); }
;             }
;             __syncthreads();
;             if (pass == 0) { for (int pc = F.wave; pc < 73; pc += NWAVES) lds_dma16(WRT + RT_STRIDE + (size_t)pc * 1024 + F.lane * 16, F.lds + pc * 1024); }
;             else if (row0 + 16 * step < T) { for (int pc = F.wave; pc < 73; pc += NWAVES) lds_dma16(WRT + (size_t)pc * 1024 + F.lane * 16, F.lds + pc * 1024); }
	v_mfma_f32_16x16x32_bf16 v[134:137], v[90:93], v[180:183], v[134:137]
	ds_read_b128 v[180:183], v159 offset:34560
	s_waitcnt lgkmcnt(5)
	v_mfma_f32_16x16x32_bf16 v[138:141], v[90:93], v[184:187], v[138:141]
	ds_read_b128 v[184:187], v159 offset:42816
	s_waitcnt lgkmcnt(5)
	v_mfma_f32_16x16x32_bf16 v[130:133], v[94:97], v[190:193], v[130:133]
	ds_read_b128 v[190:193], v159 offset:1600
	s_waitcnt lgkmcnt(5)
	v_mfma_f32_16x16x32_bf16 v[134:137], v[94:97], v[194:197], v[134:137]
	ds_read_b128 v[194:197], v159 offset:34624
	s_waitcnt lgkmcnt(5)
	v_mfma_f32_16x16x32_bf16 v[138:141], v[94:97], v[198:201], v[138:141]
	ds_read_b128 v[198:201], v159 offset:42880
	s_waitcnt lgkmcnt(5)
	v_mfma_f32_16x16x32_bf16 v[130:133], v[98:101], v[176:179], v[130:133]
	ds_read_b128 v[176:179], v159 offset:1664
	s_waitcnt lgkmcnt(5)
	v_mfma_f32_16x16x32_bf16 v[134:137], v[98:101], v[180:183], v[134:137]
	ds_read_b128 v[180:183], v159 offset:34688
	s_waitcnt lgkmcnt(5)
	v_mfma_f32_16x16x32_bf16 v[138:141], v[98:101], v[184:187], v[138:141]
	ds_read_b128 v[184:187], v159 offset:42944
	s_waitcnt lgkmcnt(5)
	v_mfma_f32_16x16x32_bf16 v[130:133], v[102:105], v[190:193], v[130:133]
	ds_read_b128 v[190:193], v159 offset:1728
	s_waitcnt lgkmcnt(5)
	v_mfma_f32_16x16x32_bf16 v[134:137], v[102:105], v[194:197], v[134:137]
	ds_read_b128 v[194:197], v159 offset:34752
	s_waitcnt lgkmcnt(5)
	v_mfma_f32_16x16x32_bf16 v[138:141], v[102:105], v[198:201], v[138:141]
	ds_read_b128 v[198:201], v159 offset:43008
	s_waitcnt lgkmcnt(5)
	v_mfma_f32_16x16x32_bf16 v[130:133], v[106:109], v[176:179], v[130:133]
	ds_read_b128 v[176:179], v159 offset:1792
	s_waitcnt lgkmcnt(5)
	v_mfma_f32_16x16x32_bf16 v[134:137], v[106:109], v[180:183], v[134:137]
	ds_read_b128 v[180:183], v159 offset:34816
	s_waitcnt lgkmcnt(5)
	v_mfma_f32_16x16x32_bf16 v[138:141], v[106:109], v[184:187], v[138:141]
	ds_read_b128 v[184:187], v159 offset:43072
	s_waitcnt lgkmcnt(5)
	v_mfma_f32_16x16x32_bf16 v[130:133], v[110:113], v[190:193], v[130:133]
	ds_read_b128 v[190:193], v159 offset:1856
	s_waitcnt lgkmcnt(5)
	v_mfma_f32_16x16x32_bf16 v[134:137], v[110:113], v[194:197], v[134:137]
	ds_read_b128 v[194:197], v159 offset:34880
	s_waitcnt lgkmcnt(5)
	v_mfma_f32_16x16x32_bf16 v[138:141], v[110:113], v[198:201], v[138:141]
	ds_read_b128 v[198:201], v159 offset:43136
	s_waitcnt lgkmcnt(5)
	v_mfma_f32_16x16x32_bf16 v[130:133], v[114:117], v[176:179], v[130:133]
	ds_read_b128 v[176:179], v159 offset:1920
	s_waitcnt lgkmcnt(5)
	v_mfma_f32_16x16x32_bf16 v[134:137], v[114:117], v[180:183], v[134:137]
	ds_read_b128 v[180:183], v159 offset:34944
	s_waitcnt lgkmcnt(5)
	v_mfma_f32_16x16x32_bf16 v[138:141], v[114:117], v[184:187], v[138:141]
	ds_read_b128 v[184:187], v159 offset:43200
	s_waitcnt lgkmcnt(5)
	v_mfma_f32_16x16x32_bf16 v[130:133], v[118:121], v[190:193], v[130:133]
	ds_read_b128 v[190:193], v159 offset:1984
	s_waitcnt lgkmcnt(5)
	v_mfma_f32_16x16x32_bf16 v[134:137], v[118:121], v[194:197], v[134:137]
	ds_read_b128 v[194:197], v159 offset:35008
	s_waitcnt lgkmcnt(5)
	v_mfma_f32_16x16x32_bf16 v[138:141], v[118:121], v[198:201], v[138:141]
	ds_read_b128 v[198:201], v159 offset:43264
	s_waitcnt lgkmcnt(5)
	v_mfma_f32_16x16x32_bf16 v[130:133], v[122:125], v[176:179], v[130:133]
	s_waitcnt lgkmcnt(4)
	v_mfma_f32_16x16x32_bf16 v[134:137], v[122:125], v[180:183], v[134:137]
	s_waitcnt lgkmcnt(3)
	v_mfma_f32_16x16x32_bf16 v[138:141], v[122:125], v[184:187], v[138:141]
	s_waitcnt lgkmcnt(2)
	v_mfma_f32_16x16x32_bf16 v[130:133], v[126:129], v[190:193], v[130:133]
	s_waitcnt lgkmcnt(1)
	v_mfma_f32_16x16x32_bf16 v[134:137], v[126:129], v[194:197], v[134:137]
	s_waitcnt lgkmcnt(0)
	s_barrier
	v_mfma_f32_16x16x32_bf16 v[138:141], v[126:129], v[198:201], v[138:141]
	s_cbranch_vccz .LBB0_1037
	s_andn2_b64 vcc, exec, s[18:19]
	s_mov_b32 s3, s58
	s_mov_b32 s6, s55
	v_mov_b64_e32 v[154:155], v[148:149]
	s_cbranch_vccnz .LBB0_1036
